# k3: assign stores sc0 sc1 (do not keep lines in L2) + per-XCD L2 warm-up of codebook fragments before main loop
# speedup vs baseline: 1.0639x; 1.0216x over previous
.LBB2_414:
	s_movk_i32 s0, 0xc00
	v_mov_b64_e32 v[26:27], s[42:43]
	v_mul_u32_u24_e32 v28, 0xc00, v154
	v_mad_i64_i32 v[26:27], s[0:1], v62, s0, v[26:27]
	v_or_b32_e32 v28, v28, v98
	v_mov_b32_e32 v99, 0
	v_lshl_add_u64 v[26:27], v[26:27], 0, v[98:99]
	v_or_b32_e32 v29, 0x10000, v28
	global_store_dwordx4 v[26:27], v[22:25], off
	ds_write_b128 v29, v[22:25]
	v_sub_f32_e32 v10, v10, v22
	v_or_b32_e32 v22, v101, v154
	v_sub_f32_e32 v11, v11, v23
	v_add_u32_e32 v23, v22, v102
	v_lshl_or_b32 v23, v23, 4, v103
	ds_write_b32 v23, v10
	v_add_u32_e32 v10, v22, v104
	v_lshl_or_b32 v10, v10, 4, v105
	ds_write_b32 v10, v11
	v_or_b32_e32 v10, v106, v154
	v_add_u32_e32 v10, v10, v107
	v_sub_f32_e32 v12, v12, v24
	v_lshl_or_b32 v10, v10, 4, v108
	ds_write_b32 v10, v12
	v_or_b32_e32 v10, v109, v154
	v_add_u32_e32 v10, v10, v110
	v_sub_f32_e32 v13, v13, v25
	v_lshl_or_b32 v10, v10, 4, v111
	ds_write_b32 v10, v13
	v_add_u32_e32 v10, 0x10400, v28
	ds_write_b128 v10, v[18:21]
	v_sub_f32_e32 v10, v6, v18
	v_sub_f32_e32 v11, v7, v19
	v_pk_add_f32 v[6:7], v[8:9], v[20:21] neg_lo:[0,1] neg_hi:[0,1]
	v_or_b32_e32 v8, v112, v154
	v_add_u32_e32 v9, v8, v113
	v_add_u32_e32 v8, v8, v115
	v_lshl_or_b32 v9, v9, 4, v114
	v_lshl_or_b32 v8, v8, 4, v116
	ds_write_b32 v9, v10
	ds_write_b32 v8, v11
	v_or_b32_e32 v8, v117, v154
	v_add_u32_e32 v8, v8, v118
	v_lshl_or_b32 v8, v8, 4, v119
	ds_write_b32 v8, v6
	v_or_b32_e32 v6, v120, v154
	v_add_u32_e32 v6, v6, v121
	v_lshl_or_b32 v6, v6, 4, v122
	ds_write_b32 v6, v7
	v_add_u32_e32 v6, 0x10800, v28
	ds_write_b128 v6, v[14:17]
	v_or_b32_e32 v6, v123, v154
	v_add_u32_e32 v7, v6, v124
	v_pk_add_f32 v[2:3], v[2:3], v[14:15] neg_lo:[0,1] neg_hi:[0,1]
	v_lshl_or_b32 v7, v7, 4, v125
	ds_write_b32 v7, v2
	v_add_u32_e32 v2, v6, v126
	v_lshl_or_b32 v2, v2, 4, v127
	ds_write_b32 v2, v3
	v_or_b32_e32 v2, v133, v154
	v_add_u32_e32 v2, v2, v134
	v_pk_add_f32 v[4:5], v[4:5], v[16:17] neg_lo:[0,1] neg_hi:[0,1]
	v_lshl_or_b32 v2, v2, 4, v63
	ds_write_b32 v2, v4
	v_or_b32_e32 v2, v135, v154
	v_add_u32_e32 v2, v2, v132
	v_lshl_or_b32 v2, v2, 4, v136
	v_add_lshl_u32 v4, v100, v154, 4
	s_mov_b32 s5, 0
	s_mov_b32 s4, 1.0
	ds_write_b32 v2, v5
	v_mov_b64_e32 v[2:3], s[4:5]
	v_add_u32_e32 v4, 8, v4
	s_waitcnt vmcnt(1)
	v_lshlrev_b32_e32 v40, 9, v150
	ds_write2st64_b64 v4, v[2:3], v[2:3] offset1:64
	v_or_b32_e32 v2, v40, v128
	v_lshlrev_b32_e32 v98, 4, v2
	v_lshl_add_u64 v[100:101], s[40:41], 0, v[98:99]
	s_mov_b64 s[0:1], 0x787000
	v_lshl_add_u64 v[34:35], v[100:101], 0, s[0:1]
	s_mov_b32 s0, 0x788000
	v_add_co_u32_e32 v36, vcc, s0, v100
	global_store_dwordx4 v[26:27], v[18:21], off offset:1024
	global_store_dwordx4 v[26:27], v[14:17], off offset:2048
	s_waitcnt lgkmcnt(0)
	s_barrier
	v_addc_co_u32_e32 v37, vcc, 0, v101, vcc
	s_lshr_b32 s59, s33, 4
	s_and_b32 s59, s59, 31
	s_lshl_b32 s59, s59, 15
	s_add_u32 s59, s59, 0x787000
	s_add_u32 s68, s40, s59
	s_addc_u32 s69, s41, 0
	v_lshlrev_b32_e32 v207, 6, v0
	global_load_dword v207, v207, s[68:69]
	global_load_dwordx4 v[2:5], v[34:35], off offset:1024
	global_load_dwordx4 v[10:13], v[34:35], off offset:2048
	global_load_dwordx4 v[14:17], v[34:35], off offset:3072
	global_load_dwordx4 v[6:9], v[36:37], off offset:-4096
	global_load_dwordx4 v[18:21], v[36:37], off
	global_load_dwordx4 v[22:25], v[36:37], off offset:1024
	global_load_dwordx4 v[26:29], v[36:37], off offset:2048
	global_load_dwordx4 v[30:33], v[36:37], off offset:3072
	v_and_b32_e32 v35, 15, v0
	v_lshrrev_b32_e32 v37, 4, v128
	v_lshlrev_b32_e32 v102, 2, v35
	v_lshlrev_b32_e32 v41, 2, v37
	v_lshlrev_b32_e32 v34, 4, v35
	v_cmp_gt_u32_e64 s[0:1], 6, v35
	v_mov_b32_e32 v35, v99
	v_or3_b32 v36, v34, v41, v40
	v_lshl_add_u64 v[104:105], s[44:45], 0, v[34:35]
	v_or_b32_e32 v34, v40, v34
	s_movk_i32 s4, 0x1000
	v_or3_b32 v153, v34, v41, s4
	v_or_b32_e32 v34, 0x11800, v98
	v_lshl_add_u64 v[118:119], s[40:41], 0, v[34:35]
	v_or_b32_e32 v34, 0x11400, v98
	v_lshl_add_u64 v[120:121], s[40:41], 0, v[34:35]
	v_or_b32_e32 v34, 0x11000, v98
	ds_read2st64_b32 v[132:133], v36 offset1:1
	v_or_b32_e32 v36, s33, v41
	v_lshl_add_u64 v[122:123], s[40:41], 0, v[34:35]
	v_or_b32_e32 v34, 0x10c00, v98
	v_or_b32_e32 v38, 1, v36
	v_lshl_add_u64 v[124:125], s[40:41], 0, v[34:35]
	v_or_b32_e32 v34, 0x10800, v98
	v_mul_u32_u24_e32 v152, 0x3000, v37
	v_ashrrev_i32_e32 v37, 31, v36
	v_ashrrev_i32_e32 v39, 31, v38
	v_lshl_add_u64 v[126:127], s[40:41], 0, v[34:35]
	v_or_b32_e32 v34, 0x10400, v98
	v_mov_b32_e32 v103, v99
	v_lshlrev_b64 v[108:109], 17, v[36:37]
	v_lshlrev_b64 v[110:111], 17, v[38:39]
	v_or_b32_e32 v38, 2, v36
	v_or_b32_e32 v36, 3, v36
	v_lshl_add_u64 v[128:129], s[40:41], 0, v[34:35]
	v_mul_u32_u24_e32 v34, 24, v150
	v_lshl_add_u64 v[106:107], s[38:39], 0, v[102:103]
	v_ashrrev_i32_e32 v39, 31, v38
	v_ashrrev_i32_e32 v37, 31, v36
	v_lshlrev_b32_e32 v103, 2, v0
	v_or_b32_e32 v98, 0x11c00, v98
	v_or_b32_e32 v34, v152, v34
	v_lshlrev_b64 v[112:113], 17, v[38:39]
	v_lshlrev_b64 v[114:115], 17, v[36:37]
	v_and_b32_e32 v116, 0x700, v103
	v_mov_b32_e32 v117, v99
	v_lshl_add_u64 v[130:131], s[40:41], 0, v[98:99]
	v_add_u32_e32 v154, v34, v102
	s_mov_b64 s[6:7], 0
	s_mov_b64 s[8:9], 0x800
	v_mov_b32_e32 v155, 0x400
	v_mov_b32_e32 v159, 0
	v_mov_b32_e32 v158, 0
	v_mov_b32_e32 v157, 0
	v_mov_b32_e32 v156, 0
	s_waitcnt vmcnt(0)
	s_branch .LBB2_417

.LBB2_416:
	s_or_b64 exec, exec, s[10:11]
	v_add_f32_e32 v64, v160, v161
	v_rcp_f32_e32 v64, v64
	v_add_f32_e32 v65, v163, v164
	v_lshl_add_u64 v[96:97], v[40:41], 2, v[104:105]
	v_rcp_f32_e32 v72, v65
	v_add_f32_e32 v48, v48, v56
	v_lshl_add_u64 v[40:41], v[96:97], 0, v[108:109]
	v_pk_mul_f32 v[134:135], v[64:65], v[134:135] op_sel_hi:[0,1]
	v_pk_mul_f32 v[136:137], v[64:65], v[136:137] op_sel_hi:[0,1]
	v_rcp_f32_e32 v56, v48
	global_store_dwordx4 v[40:41], v[134:137], off sc0 sc1
	v_add_f32_e32 v48, v49, v57
	v_rcp_f32_e32 v88, v48
	v_pk_mul_f32 v[134:135], v[64:65], v[138:139] op_sel_hi:[0,1]
	v_pk_mul_f32 v[136:137], v[64:65], v[140:141] op_sel_hi:[0,1]
	global_store_dwordx4 v[40:41], v[134:137], off offset:256 sc0 sc1
	v_pk_mul_f32 v[38:39], v[56:57], v[38:39] op_sel_hi:[0,1]
	s_add_u32 s6, s6, 0x10000
	v_pk_mul_f32 v[134:135], v[64:65], v[142:143] op_sel_hi:[0,1]
	v_pk_mul_f32 v[136:137], v[64:65], v[144:145] op_sel_hi:[0,1]
	global_store_dwordx4 v[40:41], v[134:137], off offset:512 sc0 sc1
	s_addc_u32 s7, s7, 0
	s_add_i32 s5, s5, 1
	v_pk_mul_f32 v[134:135], v[64:65], v[146:147] op_sel_hi:[0,1]
	v_pk_mul_f32 v[136:137], v[64:65], v[148:149] op_sel_hi:[0,1]
	global_store_dwordx4 v[40:41], v[134:137], off offset:768 sc0 sc1
	v_pk_mul_f32 v[40:41], v[72:73], v[42:43] op_sel_hi:[0,1]
	v_pk_mul_f32 v[42:43], v[72:73], v[34:35] op_sel_hi:[0,1]
	v_lshl_add_u64 v[134:135], v[96:97], 0, v[110:111]
	global_store_dwordx4 v[134:135], v[40:43], off offset:768 sc0 sc1
	v_lshl_add_u64 v[34:35], v[96:97], 0, v[112:113]
	v_pk_mul_f32 v[80:81], v[72:73], v[90:91] op_sel_hi:[0,1]
	v_pk_mul_f32 v[40:41], v[56:57], v[46:47] op_sel_hi:[0,1]
	global_store_dwordx4 v[34:35], v[38:41], off sc0 sc1
	v_lshl_add_u64 v[42:43], v[96:97], 0, v[114:115]
	v_pk_mul_f32 v[82:83], v[72:73], v[82:83] op_sel_hi:[0,1]
	v_pk_mul_f32 v[38:39], v[56:57], v[54:55] op_sel_hi:[0,1]
	v_pk_mul_f32 v[40:41], v[56:57], v[62:63] op_sel_hi:[0,1]
	global_store_dwordx4 v[34:35], v[38:41], off offset:256 sc0 sc1
	v_pk_mul_f32 v[64:65], v[72:73], v[74:75] op_sel_hi:[0,1]
	v_pk_mul_f32 v[66:67], v[72:73], v[66:67] op_sel_hi:[0,1]
	v_pk_mul_f32 v[38:39], v[56:57], v[70:71] op_sel_hi:[0,1]
	v_pk_mul_f32 v[40:41], v[56:57], v[78:79] op_sel_hi:[0,1]
	global_store_dwordx4 v[34:35], v[38:41], off offset:512 sc0 sc1
	v_pk_mul_f32 v[48:49], v[72:73], v[58:59] op_sel_hi:[0,1]
	v_pk_mul_f32 v[50:51], v[72:73], v[50:51] op_sel_hi:[0,1]
	v_pk_mul_f32 v[38:39], v[56:57], v[86:87] op_sel_hi:[0,1]
	v_pk_mul_f32 v[40:41], v[56:57], v[94:95] op_sel_hi:[0,1]
	global_store_dwordx4 v[34:35], v[38:41], off offset:768 sc0 sc1
	v_pk_mul_f32 v[34:35], v[88:89], v[44:45] op_sel_hi:[0,1]
	v_pk_mul_f32 v[36:37], v[88:89], v[36:37] op_sel_hi:[0,1]
	v_pk_mul_f32 v[38:39], v[88:89], v[92:93] op_sel_hi:[0,1]
	v_pk_mul_f32 v[40:41], v[88:89], v[84:85] op_sel_hi:[0,1]
	global_store_dwordx4 v[42:43], v[38:41], off sc0 sc1
	v_lshl_add_u64 v[116:117], v[116:117], 0, s[8:9]
	v_add_u32_e32 v153, 0x1000, v153
	v_pk_mul_f32 v[38:39], v[88:89], v[76:77] op_sel_hi:[0,1]
	v_pk_mul_f32 v[40:41], v[88:89], v[68:69] op_sel_hi:[0,1]
	global_store_dwordx4 v[42:43], v[38:41], off offset:256 sc0 sc1
	s_cmp_eq_u32 s6, 0x100000
	v_add_u32_e32 v154, 0xc0, v154
	v_pk_mul_f32 v[38:39], v[88:89], v[60:61] op_sel_hi:[0,1]
	v_pk_mul_f32 v[40:41], v[88:89], v[52:53] op_sel_hi:[0,1]
	global_store_dwordx4 v[134:135], v[80:83], off sc0 sc1
	global_store_dwordx4 v[134:135], v[64:67], off offset:256 sc0 sc1
	global_store_dwordx4 v[134:135], v[48:51], off offset:512 sc0 sc1
	global_store_dwordx4 v[42:43], v[38:41], off offset:512 sc0 sc1
	global_store_dwordx4 v[42:43], v[34:37], off offset:768 sc0 sc1
	s_cbranch_scc1 .LBB2_422

	.amdhsa_kernel _Z7k3_mainPKhPKfS2_S2_S2_PfS3_S3_
		.amdhsa_group_segment_fixed_size 117312
		.amdhsa_private_segment_fixed_size 0
		.amdhsa_kernarg_size 64
		.amdhsa_user_sgpr_count 2
		.amdhsa_user_sgpr_dispatch_ptr 0
		.amdhsa_user_sgpr_queue_ptr 0
		.amdhsa_user_sgpr_kernarg_segment_ptr 1
		.amdhsa_user_sgpr_dispatch_id 0
		.amdhsa_user_sgpr_kernarg_preload_length 0
		.amdhsa_user_sgpr_kernarg_preload_offset 0
		.amdhsa_user_sgpr_private_segment_size 0
		.amdhsa_uses_dynamic_stack 0
		.amdhsa_enable_private_segment 0
		.amdhsa_system_sgpr_workgroup_id_x 1
		.amdhsa_system_sgpr_workgroup_id_y 0
		.amdhsa_system_sgpr_workgroup_id_z 0
		.amdhsa_system_sgpr_workgroup_info 0
		.amdhsa_system_vgpr_workitem_id 0
		.amdhsa_next_free_vgpr 208
		.amdhsa_next_free_sgpr 96
		.amdhsa_accum_offset 208
		.amdhsa_reserve_vcc 1
		.amdhsa_float_round_mode_32 0
		.amdhsa_float_round_mode_16_64 0
		.amdhsa_float_denorm_mode_32 3
		.amdhsa_float_denorm_mode_16_64 3
		.amdhsa_dx10_clamp 1
		.amdhsa_ieee_mode 1
		.amdhsa_fp16_overflow 0
		.amdhsa_tg_split 0
		.amdhsa_exception_fp_ieee_invalid_op 0
		.amdhsa_exception_fp_denorm_src 0
		.amdhsa_exception_fp_ieee_div_zero 0
		.amdhsa_exception_fp_ieee_overflow 0
		.amdhsa_exception_fp_ieee_underflow 0
		.amdhsa_exception_fp_ieee_inexact 0
		.amdhsa_exception_int_div_zero 0
	.end_amdhsa_kernel

amdhsa.kernels:
  - .agpr_count:     0
    .args:
      - .actual_access:  read_only
        .address_space:  global
        .offset:         0
        .size:           8
        .value_kind:     global_buffer
      - .actual_access:  read_only
        .address_space:  global
        .offset:         8
        .size:           8
        .value_kind:     global_buffer
      - .actual_access:  read_only
        .address_space:  global
        .offset:         16
        .size:           8
        .value_kind:     global_buffer
      - .actual_access:  write_only
        .address_space:  global
        .offset:         24
        .size:           8
        .value_kind:     global_buffer
    .group_segment_fixed_size: 0
    .kernarg_segment_align: 8
    .kernarg_segment_size: 32
    .language:       OpenCL C
    .language_version:
      - 2
      - 0
    .max_flat_workgroup_size: 256
    .name:           _Z7k0_prepPKfS0_S0_Ph
    .private_segment_fixed_size: 0
    .sgpr_count:     24
    .sgpr_spill_count: 0
    .symbol:         _Z7k0_prepPKfS0_S0_Ph.kd
    .uniform_work_group_size: 1
    .uses_dynamic_stack: false
    .vgpr_count:     31
    .vgpr_spill_count: 0
    .wavefront_size: 64
  - .agpr_count:     76
    .args:
      - .actual_access:  read_only
        .address_space:  global
        .offset:         0
        .size:           8
        .value_kind:     global_buffer
      - .actual_access:  write_only
        .address_space:  global
        .offset:         8
        .size:           8
        .value_kind:     global_buffer
    .group_segment_fixed_size: 73728
    .kernarg_segment_align: 8
    .kernarg_segment_size: 16
    .language:       OpenCL C
    .language_version:
      - 2
      - 0
    .max_flat_workgroup_size: 256
    .name:           _Z7k1_gemmPKhPf
    .private_segment_fixed_size: 0
    .sgpr_count:     18
    .sgpr_spill_count: 0
    .symbol:         _Z7k1_gemmPKhPf.kd
    .uniform_work_group_size: 1
    .uses_dynamic_stack: false
    .vgpr_count:     332
    .vgpr_spill_count: 0
    .wavefront_size: 64
  - .agpr_count:     0
    .args:
      - .actual_access:  read_only
        .address_space:  global
        .offset:         0
        .size:           8
        .value_kind:     global_buffer
      - .actual_access:  read_only
        .address_space:  global
        .offset:         8
        .size:           8
        .value_kind:     global_buffer
      - .actual_access:  read_only
        .address_space:  global
        .offset:         16
        .size:           8
        .value_kind:     global_buffer
      - .actual_access:  read_only
        .address_space:  global
        .offset:         24
        .size:           8
        .value_kind:     global_buffer
      - .actual_access:  read_only
        .address_space:  global
        .offset:         32
        .size:           8
        .value_kind:     global_buffer
      - .actual_access:  write_only
        .address_space:  global
        .offset:         40
        .size:           8
        .value_kind:     global_buffer
      - .actual_access:  write_only
        .address_space:  global
        .offset:         48
        .size:           8
        .value_kind:     global_buffer
      - .actual_access:  write_only
        .address_space:  global
        .offset:         56
        .size:           8
        .value_kind:     global_buffer
    .group_segment_fixed_size: 117312
    .kernarg_segment_align: 8
    .kernarg_segment_size: 64
    .language:       OpenCL C
    .language_version:
      - 2
      - 0
    .max_flat_workgroup_size: 512
    .name:           _Z7k3_mainPKhPKfS2_S2_S2_PfS3_S3_
    .private_segment_fixed_size: 0
    .sgpr_count:     64
    .sgpr_spill_count: 0
    .symbol:         _Z7k3_mainPKhPKfS2_S2_S2_PfS3_S3_.kd
    .uniform_work_group_size: 1
    .uses_dynamic_stack: false
    .vgpr_count:     208
    .vgpr_spill_count: 0
    .wavefront_size: 64
